# speedup vs baseline: 1.0016x; 1.0016x over previous
_Z11pam_combinePKDF16_PKfS2_S2_Pf:
	s_load_dwordx8 s[8:15], s[0:1], 0x0
	s_load_dwordx2 s[20:21], s[0:1], 0x20
	v_lshl_or_b32 v0, s2, 8, v0
	s_mov_b32 s4, 0x24924925
	s_mov_b32 s5, 0xaaaaab
	s_movk_i32 s6, 0xfe80
	s_movk_i32 s7, 0x5556
	s_movk_i32 s16, 0x180
	s_movk_i32 s17, 0x68
	v_mul_hi_u32 v1, v0, s4
	v_mad_i32_i24 v2, v1, -7, v0
	v_mul_hi_u32 v3, v1, s5
	v_mad_i32_i24 v4, v3, s6, v1
	v_lshlrev_b32_e32 v7, 4, v3
	v_mul_u32_u24_e32 v5, s7, v7
	v_lshrrev_b32_e32 v5, 16, v5
	v_add_u32_e32 v7, 15, v7
	v_mul_u32_u24_e32 v6, s7, v7
	v_lshrrev_b32_e32 v6, 16, v6
	v_sub_u32_e32 v6, v6, v5
	v_mad_u32_u24 v7, v5, s16, v4
	v_lshlrev_b32_e32 v10, 4, v2
	v_lshlrev_b32_e32 v8, 2, v7
	v_mad_u32_u24 v9, v7, s17, v10
	v_lshl_add_u32 v7, v5, 1, v5
	v_lshrrev_b32_e32 v7, 4, v7
	v_cmp_eq_u32_e32 vcc, v7, v3
	v_add_u32_e32 v7, 0x100, v3
	v_mul_u32_u24_e32 v100, 0xc8, v1
	v_cndmask_b32_e32 v7, v7, v5, vcc
	v_mad_u32_u24 v7, v7, s16, v4
	v_lshlrev_b32_e32 v11, 2, v7
	v_mad_u32_u24 v18, v7, s17, v10
	v_add_u32_e32 v12, 0x600, v8
	v_add_u32_e32 v19, 0x9c00, v9
	v_add_u32_e32 v13, 0xc00, v8
	v_add_u32_e32 v20, 0x13800, v9
	v_add_u32_e32 v14, 0x1200, v8
	v_add_u32_e32 v21, 0x1d400, v9
	v_add_u32_e32 v15, 0x1800, v8
	v_add_u32_e32 v22, 0x27000, v9
	v_add_u32_e32 v16, 0x1e00, v8
	v_add_u32_e32 v23, 0x30c00, v9
	v_mul_u32_u24_e32 v7, 0x600, v6
	v_add_u32_e32 v17, v7, v8
	v_mul_u32_u24_e32 v7, 0x9c00, v6
	v_add_u32_e32 v24, v7, v9
	v_lshl_add_u32 v100, v2, 5, v100
	v_cmp_gt_u32_e32 vcc, 6, v2
	s_nop 1
	v_cndmask_b32_e64 v7, 0, 8, vcc
	s_waitcnt lgkmcnt(0)
	s_load_dword s18, s[14:15], 0x0
	global_load_dwordx2 v[60:61], v100, s[12:13]
	v_add_u32_e32 v8, v100, v7
	v_lshl_add_u32 v9, v7, 1, v100
	v_mad_u32_u24 v10, v7, 3, v100
	global_load_dwordx2 v[62:63], v8, s[12:13]
	global_load_dwordx2 v[64:65], v9, s[12:13]
	global_load_dwordx2 v[66:67], v10, s[12:13]
	global_load_dword v25, v11, s[10:11]
	global_load_dword v26, v12, s[10:11]
	global_load_dword v27, v13, s[10:11]
	global_load_dword v28, v14, s[10:11]
	global_load_dword v29, v15, s[10:11]
	global_load_dword v30, v16, s[10:11]
	global_load_dword v31, v17, s[10:11]
	global_load_dwordx4 v[32:35], v18, s[8:9] nt
	global_load_dwordx4 v[36:39], v19, s[8:9] nt
	global_load_dwordx4 v[40:43], v20, s[8:9] nt
	global_load_dwordx4 v[44:47], v21, s[8:9] nt
	global_load_dwordx4 v[48:51], v22, s[8:9] nt
	global_load_dwordx4 v[52:55], v23, s[8:9] nt
	global_load_dwordx4 v[56:59], v24, s[8:9] nt
	v_cmp_eq_u32_e32 vcc, 6, v6
	v_mov_b32_e32 v69, 0xff61b1e6
	s_waitcnt vmcnt(7)
	v_cndmask_b32_e32 v7, v69, v31, vcc
	v_max3_f32 v8, v25, v26, v27
	v_max3_f32 v8, v8, v28, v29
	v_max3_f32 v8, v8, v30, v7
	v_max_f32_e32 v69, v69, v8
	v_sub_f32_e32 v68, v25, v69
	v_sub_f32_e32 v70, v26, v69
	v_sub_f32_e32 v72, v27, v69
	v_sub_f32_e32 v74, v28, v69
	v_sub_f32_e32 v76, v29, v69
	v_sub_f32_e32 v78, v30, v69
	v_sub_f32_e32 v80, v31, v69
	v_exp_f32_e32 v68, v68
	v_exp_f32_e32 v70, v70
	v_exp_f32_e32 v72, v72
	v_exp_f32_e32 v74, v74
	v_exp_f32_e32 v76, v76
	v_exp_f32_e32 v78, v78
	v_exp_f32_e32 v80, v80
	s_nop 0
	v_cndmask_b32_e32 v80, 0, v80, vcc
	v_add_f32_e32 v71, v68, v70
	v_add_f32_e32 v71, v71, v72
	v_add_f32_e32 v71, v71, v74
	v_add_f32_e32 v71, v71, v76
	v_add_f32_e32 v71, v71, v78
	v_add_f32_e32 v71, v71, v80
	v_div_scale_f32 v73, s[22:23], v71, v71, 1.0
	v_rcp_f32_e32 v75, v73
	s_nop 0
	v_fma_f32 v77, -v73, v75, 1.0
	v_fmac_f32_e32 v75, v77, v75
	v_div_scale_f32 v77, vcc, 1.0, v71, 1.0
	v_mul_f32_e32 v79, v77, v75
	v_fma_f32 v81, -v73, v79, v77
	v_fmac_f32_e32 v79, v81, v75
	v_fma_f32 v73, -v73, v79, v77
	s_nop 1
	v_div_fmas_f32 v73, v73, v75, v79
	v_div_fixup_f32 v82, v73, v71, 1.0
	s_waitcnt vmcnt(6)
	v_cvt_f32_f16_sdwa v93, v32 dst_sel:DWORD dst_unused:UNUSED_PAD src0_sel:WORD_1
	v_cvt_f32_f16_sdwa v95, v33 dst_sel:DWORD dst_unused:UNUSED_PAD src0_sel:WORD_1
	v_cvt_f32_f16_sdwa v97, v34 dst_sel:DWORD dst_unused:UNUSED_PAD src0_sel:WORD_1
	v_cvt_f32_f16_sdwa v99, v35 dst_sel:DWORD dst_unused:UNUSED_PAD src0_sel:WORD_1
	v_cvt_f32_f16_e32 v92, v32
	v_cvt_f32_f16_e32 v94, v33
	v_cvt_f32_f16_e32 v96, v34
	v_cvt_f32_f16_e32 v98, v35
	v_pk_fma_f32 v[84:85], v[68:69], v[92:93], 0 op_sel_hi:[0,1,0]
	v_pk_fma_f32 v[86:87], v[68:69], v[94:95], 0 op_sel_hi:[0,1,0]
	v_pk_fma_f32 v[88:89], v[68:69], v[96:97], 0 op_sel_hi:[0,1,0]
	v_pk_fma_f32 v[90:91], v[68:69], v[98:99], 0 op_sel_hi:[0,1,0]
	s_waitcnt vmcnt(5)
	v_cvt_f32_f16_sdwa v93, v36 dst_sel:DWORD dst_unused:UNUSED_PAD src0_sel:WORD_1
	v_cvt_f32_f16_sdwa v95, v37 dst_sel:DWORD dst_unused:UNUSED_PAD src0_sel:WORD_1
	v_cvt_f32_f16_sdwa v97, v38 dst_sel:DWORD dst_unused:UNUSED_PAD src0_sel:WORD_1
	v_cvt_f32_f16_sdwa v99, v39 dst_sel:DWORD dst_unused:UNUSED_PAD src0_sel:WORD_1
	v_cvt_f32_f16_e32 v92, v36
	v_cvt_f32_f16_e32 v94, v37
	v_cvt_f32_f16_e32 v96, v38
	v_cvt_f32_f16_e32 v98, v39
	v_pk_fma_f32 v[84:85], v[70:71], v[92:93], v[84:85] op_sel_hi:[0,1,1]
	v_pk_fma_f32 v[86:87], v[70:71], v[94:95], v[86:87] op_sel_hi:[0,1,1]
	v_pk_fma_f32 v[88:89], v[70:71], v[96:97], v[88:89] op_sel_hi:[0,1,1]
	v_pk_fma_f32 v[90:91], v[70:71], v[98:99], v[90:91] op_sel_hi:[0,1,1]
	s_waitcnt vmcnt(4)
	v_cvt_f32_f16_sdwa v93, v40 dst_sel:DWORD dst_unused:UNUSED_PAD src0_sel:WORD_1
	v_cvt_f32_f16_sdwa v95, v41 dst_sel:DWORD dst_unused:UNUSED_PAD src0_sel:WORD_1
	v_cvt_f32_f16_sdwa v97, v42 dst_sel:DWORD dst_unused:UNUSED_PAD src0_sel:WORD_1
	v_cvt_f32_f16_sdwa v99, v43 dst_sel:DWORD dst_unused:UNUSED_PAD src0_sel:WORD_1
	v_cvt_f32_f16_e32 v92, v40
	v_cvt_f32_f16_e32 v94, v41
	v_cvt_f32_f16_e32 v96, v42
	v_cvt_f32_f16_e32 v98, v43
	v_pk_fma_f32 v[84:85], v[72:73], v[92:93], v[84:85] op_sel_hi:[0,1,1]
	v_pk_fma_f32 v[86:87], v[72:73], v[94:95], v[86:87] op_sel_hi:[0,1,1]
	v_pk_fma_f32 v[88:89], v[72:73], v[96:97], v[88:89] op_sel_hi:[0,1,1]
	v_pk_fma_f32 v[90:91], v[72:73], v[98:99], v[90:91] op_sel_hi:[0,1,1]
	s_waitcnt vmcnt(3)
	v_cvt_f32_f16_sdwa v93, v44 dst_sel:DWORD dst_unused:UNUSED_PAD src0_sel:WORD_1
	v_cvt_f32_f16_sdwa v95, v45 dst_sel:DWORD dst_unused:UNUSED_PAD src0_sel:WORD_1
	v_cvt_f32_f16_sdwa v97, v46 dst_sel:DWORD dst_unused:UNUSED_PAD src0_sel:WORD_1
	v_cvt_f32_f16_sdwa v99, v47 dst_sel:DWORD dst_unused:UNUSED_PAD src0_sel:WORD_1
	v_cvt_f32_f16_e32 v92, v44
	v_cvt_f32_f16_e32 v94, v45
	v_cvt_f32_f16_e32 v96, v46
	v_cvt_f32_f16_e32 v98, v47
	v_pk_fma_f32 v[84:85], v[74:75], v[92:93], v[84:85] op_sel_hi:[0,1,1]
	v_pk_fma_f32 v[86:87], v[74:75], v[94:95], v[86:87] op_sel_hi:[0,1,1]
	v_pk_fma_f32 v[88:89], v[74:75], v[96:97], v[88:89] op_sel_hi:[0,1,1]
	v_pk_fma_f32 v[90:91], v[74:75], v[98:99], v[90:91] op_sel_hi:[0,1,1]
	s_waitcnt vmcnt(2)
	v_cvt_f32_f16_sdwa v93, v48 dst_sel:DWORD dst_unused:UNUSED_PAD src0_sel:WORD_1
	v_cvt_f32_f16_sdwa v95, v49 dst_sel:DWORD dst_unused:UNUSED_PAD src0_sel:WORD_1
	v_cvt_f32_f16_sdwa v97, v50 dst_sel:DWORD dst_unused:UNUSED_PAD src0_sel:WORD_1
	v_cvt_f32_f16_sdwa v99, v51 dst_sel:DWORD dst_unused:UNUSED_PAD src0_sel:WORD_1
	v_cvt_f32_f16_e32 v92, v48
	v_cvt_f32_f16_e32 v94, v49
	v_cvt_f32_f16_e32 v96, v50
	v_cvt_f32_f16_e32 v98, v51
	v_pk_fma_f32 v[84:85], v[76:77], v[92:93], v[84:85] op_sel_hi:[0,1,1]
	v_pk_fma_f32 v[86:87], v[76:77], v[94:95], v[86:87] op_sel_hi:[0,1,1]
	v_pk_fma_f32 v[88:89], v[76:77], v[96:97], v[88:89] op_sel_hi:[0,1,1]
	v_pk_fma_f32 v[90:91], v[76:77], v[98:99], v[90:91] op_sel_hi:[0,1,1]
	s_waitcnt vmcnt(1)
	v_cvt_f32_f16_sdwa v93, v52 dst_sel:DWORD dst_unused:UNUSED_PAD src0_sel:WORD_1
	v_cvt_f32_f16_sdwa v95, v53 dst_sel:DWORD dst_unused:UNUSED_PAD src0_sel:WORD_1
	v_cvt_f32_f16_sdwa v97, v54 dst_sel:DWORD dst_unused:UNUSED_PAD src0_sel:WORD_1
	v_cvt_f32_f16_sdwa v99, v55 dst_sel:DWORD dst_unused:UNUSED_PAD src0_sel:WORD_1
	v_cvt_f32_f16_e32 v92, v52
	v_cvt_f32_f16_e32 v94, v53
	v_cvt_f32_f16_e32 v96, v54
	v_cvt_f32_f16_e32 v98, v55
	v_pk_fma_f32 v[84:85], v[78:79], v[92:93], v[84:85] op_sel_hi:[0,1,1]
	v_pk_fma_f32 v[86:87], v[78:79], v[94:95], v[86:87] op_sel_hi:[0,1,1]
	v_pk_fma_f32 v[88:89], v[78:79], v[96:97], v[88:89] op_sel_hi:[0,1,1]
	v_pk_fma_f32 v[90:91], v[78:79], v[98:99], v[90:91] op_sel_hi:[0,1,1]
	s_waitcnt vmcnt(0)
	v_cvt_f32_f16_sdwa v93, v56 dst_sel:DWORD dst_unused:UNUSED_PAD src0_sel:WORD_1
	v_cvt_f32_f16_sdwa v95, v57 dst_sel:DWORD dst_unused:UNUSED_PAD src0_sel:WORD_1
	v_cvt_f32_f16_sdwa v97, v58 dst_sel:DWORD dst_unused:UNUSED_PAD src0_sel:WORD_1
	v_cvt_f32_f16_sdwa v99, v59 dst_sel:DWORD dst_unused:UNUSED_PAD src0_sel:WORD_1
	v_cvt_f32_f16_e32 v92, v56
	v_cvt_f32_f16_e32 v94, v57
	v_cvt_f32_f16_e32 v96, v58
	v_cvt_f32_f16_e32 v98, v59
	v_pk_fma_f32 v[84:85], v[80:81], v[92:93], v[84:85] op_sel_hi:[0,1,1]
	v_pk_fma_f32 v[86:87], v[80:81], v[94:95], v[86:87] op_sel_hi:[0,1,1]
	v_pk_fma_f32 v[88:89], v[80:81], v[96:97], v[88:89] op_sel_hi:[0,1,1]
	v_pk_fma_f32 v[90:91], v[80:81], v[98:99], v[90:91] op_sel_hi:[0,1,1]
	v_pk_mul_f32 v[84:85], v[82:83], v[84:85] op_sel_hi:[0,1]
	v_pk_mul_f32 v[86:87], v[82:83], v[86:87] op_sel_hi:[0,1]
	v_pk_mul_f32 v[88:89], v[82:83], v[88:89] op_sel_hi:[0,1]
	v_pk_mul_f32 v[90:91], v[82:83], v[90:91] op_sel_hi:[0,1]
	s_waitcnt vmcnt(0) lgkmcnt(0)
	s_mov_b32 s19, s18
	v_pk_fma_f32 v[84:85], s[18:19], v[84:85], v[60:61]
	v_pk_fma_f32 v[86:87], s[18:19], v[86:87], v[62:63]
	v_pk_fma_f32 v[88:89], s[18:19], v[88:89], v[64:65]
	v_pk_fma_f32 v[90:91], s[18:19], v[90:91], v[66:67]
	v_cmp_gt_u32_e32 vcc, 6, v2
	global_store_dwordx2 v100, v[84:85], s[20:21]
	s_and_b64 exec, exec, vcc
	global_store_dwordx4 v100, v[86:89], s[20:21] offset:8
	global_store_dwordx2 v100, v[90:91], s[20:21] offset:24
	s_endpgm

	.amdhsa_kernel _Z11pam_combinePKDF16_PKfS2_S2_Pf
		.amdhsa_group_segment_fixed_size 0
		.amdhsa_private_segment_fixed_size 0
		.amdhsa_kernarg_size 40
		.amdhsa_user_sgpr_count 2
		.amdhsa_user_sgpr_dispatch_ptr 0
		.amdhsa_user_sgpr_queue_ptr 0
		.amdhsa_user_sgpr_kernarg_segment_ptr 1
		.amdhsa_user_sgpr_dispatch_id 0
		.amdhsa_user_sgpr_kernarg_preload_length 0
		.amdhsa_user_sgpr_kernarg_preload_offset 0
		.amdhsa_user_sgpr_private_segment_size 0
		.amdhsa_uses_dynamic_stack 0
		.amdhsa_enable_private_segment 0
		.amdhsa_system_sgpr_workgroup_id_x 1
		.amdhsa_system_sgpr_workgroup_id_y 0
		.amdhsa_system_sgpr_workgroup_id_z 0
		.amdhsa_system_sgpr_workgroup_info 0
		.amdhsa_system_vgpr_workitem_id 0
		.amdhsa_next_free_vgpr 104
		.amdhsa_next_free_sgpr 32
		.amdhsa_accum_offset 104
		.amdhsa_reserve_vcc 1
		.amdhsa_float_round_mode_32 0
		.amdhsa_float_round_mode_16_64 0
		.amdhsa_float_denorm_mode_32 3
		.amdhsa_float_denorm_mode_16_64 3
		.amdhsa_dx10_clamp 1
		.amdhsa_ieee_mode 1
		.amdhsa_fp16_overflow 0
		.amdhsa_tg_split 0
		.amdhsa_exception_fp_ieee_invalid_op 0
		.amdhsa_exception_fp_denorm_src 0
		.amdhsa_exception_fp_ieee_div_zero 0
		.amdhsa_exception_fp_ieee_overflow 0
		.amdhsa_exception_fp_ieee_underflow 0
		.amdhsa_exception_fp_ieee_inexact 0
		.amdhsa_exception_int_div_zero 0
	.end_amdhsa_kernel

amdhsa.kernels:
  - .agpr_count:     0
    .args:
      - .actual_access:  read_only
        .address_space:  global
        .offset:         0
        .size:           8
        .value_kind:     global_buffer
      - .actual_access:  read_only
        .address_space:  global
        .offset:         8
        .size:           8
        .value_kind:     global_buffer
      - .actual_access:  read_only
        .address_space:  global
        .offset:         16
        .size:           8
        .value_kind:     global_buffer
      - .actual_access:  read_only
        .address_space:  global
        .offset:         24
        .size:           8
        .value_kind:     global_buffer
      - .actual_access:  write_only
        .address_space:  global
        .offset:         32
        .size:           8
        .value_kind:     global_buffer
      - .actual_access:  write_only
        .address_space:  global
        .offset:         40
        .size:           8
        .value_kind:     global_buffer
      - .actual_access:  write_only
        .address_space:  global
        .offset:         48
        .size:           8
        .value_kind:     global_buffer
      - .actual_access:  write_only
        .address_space:  global
        .offset:         56
        .size:           8
        .value_kind:     global_buffer
      - .actual_access:  write_only
        .address_space:  global
        .offset:         64
        .size:           8
        .value_kind:     global_buffer
    .group_segment_fixed_size: 29184
    .kernarg_segment_align: 8
    .kernarg_segment_size: 72
    .language:       OpenCL C
    .language_version:
      - 2
      - 0
    .max_flat_workgroup_size: 256
    .name:           _Z8pam_prepPKfS0_S0_S0_PDv4_jS2_S2_PfS3_
    .private_segment_fixed_size: 0
    .sgpr_count:     28
    .sgpr_spill_count: 0
    .symbol:         _Z8pam_prepPKfS0_S0_S0_PDv4_jS2_S2_PfS3_.kd
    .uniform_work_group_size: 1
    .uses_dynamic_stack: false
    .vgpr_count:     168
    .vgpr_spill_count: 0
    .wavefront_size: 64
  - .agpr_count:     0
    .args:
      - .address_space:  global
        .offset:         0
        .size:           8
        .value_kind:     global_buffer
      - .actual_access:  read_only
        .address_space:  global
        .offset:         8
        .size:           8
        .value_kind:     global_buffer
      - .address_space:  global
        .offset:         16
        .size:           8
        .value_kind:     global_buffer
      - .actual_access:  read_only
        .address_space:  global
        .offset:         24
        .size:           8
        .value_kind:     global_buffer
      - .actual_access:  read_only
        .address_space:  global
        .offset:         32
        .size:           8
        .value_kind:     global_buffer
      - .actual_access:  write_only
        .address_space:  global
        .offset:         40
        .size:           8
        .value_kind:     global_buffer
      - .actual_access:  write_only
        .address_space:  global
        .offset:         48
        .size:           8
        .value_kind:     global_buffer
    .group_segment_fixed_size: 133120
    .kernarg_segment_align: 8
    .kernarg_segment_size: 56
    .language:       OpenCL C
    .language_version:
      - 2
      - 0
    .max_flat_workgroup_size: 768
    .name:           _Z8pam_mainPKDv4_jS1_S1_PKfS3_PDF16_Pf
    .private_segment_fixed_size: 0
    .sgpr_count:     52
    .sgpr_spill_count: 0
    .symbol:         _Z8pam_mainPKDv4_jS1_S1_PKfS3_PDF16_Pf.kd
    .uniform_work_group_size: 1
    .uses_dynamic_stack: false
    .vgpr_count:     152
    .vgpr_spill_count: 0
    .wavefront_size: 64
  - .agpr_count:     0
    .args:
      - .actual_access:  read_only
        .address_space:  global
        .offset:         0
        .size:           8
        .value_kind:     global_buffer
      - .actual_access:  read_only
        .address_space:  global
        .offset:         8
        .size:           8
        .value_kind:     global_buffer
      - .actual_access:  read_only
        .address_space:  global
        .offset:         16
        .size:           8
        .value_kind:     global_buffer
      - .actual_access:  read_only
        .address_space:  global
        .offset:         24
        .size:           8
        .value_kind:     global_buffer
      - .actual_access:  write_only
        .address_space:  global
        .offset:         32
        .size:           8
        .value_kind:     global_buffer
    .group_segment_fixed_size: 0
    .kernarg_segment_align: 8
    .kernarg_segment_size: 40
    .language:       OpenCL C
    .language_version:
      - 2
      - 0
    .max_flat_workgroup_size: 256
    .name:           _Z11pam_combinePKDF16_PKfS2_S2_Pf
    .private_segment_fixed_size: 0
    .sgpr_count:     38
    .sgpr_spill_count: 0
    .symbol:         _Z11pam_combinePKDF16_PKfS2_S2_Pf.kd
    .uniform_work_group_size: 1
    .uses_dynamic_stack: false
    .vgpr_count:     104
    .vgpr_spill_count: 0
    .wavefront_size: 64
